# speedup vs baseline: 1.0059x; 1.0059x over previous
_Z6k_distPKyPKfS2_PK15HIP_vector_typeIjLj4EEPf:
	s_load_dwordx4 s[4:7], s[0:1], 0x0
	s_load_dwordx2 s[8:9], s[0:1], 0x10
	s_lshl_b32 s3, s2, 10
	v_or_b32_e32 v4, s3, v0
	v_ashrrev_i32_e32 v5, 31, v4
	s_waitcnt lgkmcnt(0)
	v_lshl_add_u64 v[2:3], v[4:5], 3, s[4:5]
	global_load_dwordx2 v[2:3], v[2:3], off
	s_ashr_i32 s4, s3, 31
	v_mov_b32_e32 v1, s4
	v_lshlrev_b64 v[4:5], 2, v[4:5]
	v_lshl_add_u64 v[6:7], s[6:7], 0, v[4:5]
	v_lshl_add_u64 v[4:5], s[8:9], 0, v[4:5]
	global_load_dword v15, v[6:7], off
	global_load_dword v13, v[4:5], off
	s_load_dwordx2 s[4:5], s[0:1], 0x20
	s_waitcnt vmcnt(2)
	v_ashrrev_i32_e32 v9, 31, v2
	v_sub_co_u32_e32 v8, vcc, s3, v2
	s_mov_b32 s3, 0x3a83126f
	s_nop 0
	v_subb_co_u32_e32 v9, vcc, v1, v9, vcc
	v_lshlrev_b64 v[8:9], 2, v[8:9]
	v_lshl_add_u64 v[10:11], s[6:7], 0, v[8:9]
	v_lshl_add_u64 v[8:9], s[8:9], 0, v[8:9]
	global_load_dword v12, v[10:11], off offset:4092
	global_load_dword v14, v[8:9], off offset:4092
	v_bfrev_b32_e32 v4, 1
	v_cmp_lt_i64_e32 vcc, -1, v[2:3]
	s_waitcnt vmcnt(1)
	v_add_f32_e32 v1, v15, v12
	v_cndmask_b32_e64 v4, v4, -1, vcc
	v_xor_b32_e32 v3, v4, v3
	s_waitcnt vmcnt(0)
	v_sub_f32_e32 v4, v13, v14
	v_fmac_f32_e32 v1, -2.0, v3
	v_fmamk_f32 v1, v4, 0x32abcc77, v1
	v_add_f32_e32 v3, 0x29669595, v1
	v_cmp_gt_f32_e32 vcc, s3, v3
	s_and_saveexec_b64 s[6:7], vcc
	s_cbranch_execz .LBB1_3
	s_load_dwordx2 s[0:1], s[0:1], 0x18
	v_sub_u32_e32 v1, 0x3ff, v2
	s_lshl_b32 s2, s2, 5
	v_lshrrev_b32_e32 v2, 5, v0
	v_or_b32_e32 v2, s2, v2
	v_ashrrev_i32_e32 v3, 31, v2
	v_ashrrev_i32_e32 v4, 5, v1
	v_add_u32_e32 v6, s2, v4
	v_lshlrev_b64 v[2:3], 15, v[2:3]
	v_ashrrev_i32_e32 v7, 31, v6
	s_waitcnt lgkmcnt(0)
	v_lshl_add_u64 v[4:5], s[0:1], 0, v[2:3]
	v_lshlrev_b32_e32 v2, 4, v0
	v_and_b32_e32 v2, 0x1f0, v2
	v_mov_b32_e32 v3, 0
	v_lshlrev_b64 v[6:7], 15, v[6:7]
	v_lshlrev_b32_e32 v1, 4, v1
	v_lshl_add_u64 v[4:5], v[4:5], 0, v[2:3]
	v_lshl_add_u64 v[6:7], s[0:1], 0, v[6:7]
	v_and_b32_e32 v2, 0x1f0, v1
	v_lshl_add_u64 v[6:7], v[6:7], 0, v[2:3]
	s_mov_b32 s1, 0
	s_mov_b32 s2, 0
	s_mov_b32 s3, 0

.LBB2_4:
	s_endpgm
	s_nop 0
	s_nop 0
	s_nop 0
	s_nop 0
	s_nop 0
	s_nop 0
	s_nop 0
	s_nop 0
	s_nop 0
	s_nop 0
	s_nop 0
	s_nop 0
	s_nop 0
	s_nop 0
	s_nop 0
	s_nop 0
	s_nop 0
	s_nop 0
	s_nop 0
	s_nop 0
	s_nop 0
	s_nop 0
	s_nop 0
	s_nop 0
	s_nop 0
	s_nop 0
	s_nop 0
	s_nop 0
	s_nop 0
	s_nop 0
	s_nop 0
	s_nop 0
	s_nop 0
	s_nop 0
	s_nop 0
	s_nop 0
	s_nop 0
	s_nop 0
	s_nop 0
	s_nop 0
	s_nop 0
	s_nop 0
	s_nop 0
	s_nop 0
	s_nop 0
	s_nop 0
	s_nop 0
	s_endpgm
